# P9 K-loop back-edge rotation (7.11): counter/address scalar block moved in front of the loop-back barrier, exit path gets its own barrier
# speedup vs baseline: 1.0001x; 1.0001x over previous
.Lp9_pw2:
	s_waitcnt vmcnt(16)
	s_waitcnt lgkmcnt(0)
	s_barrier
	s_setprio 1
	s_waitcnt lgkmcnt(0)
	v_mfma_f32_16x16x128_f8f6f4 v[94:97], v[18:25], v[198:205], 0
	v_mfma_f32_16x16x128_f8f6f4 v[86:89], v[26:33], v[198:205], 0
	v_mfma_f32_16x16x128_f8f6f4 v[78:81], v[18:25], v[206:213], 0
	v_mfma_f32_16x16x128_f8f6f4 v[70:73], v[26:33], v[206:213], 0
	v_mfma_f32_16x16x128_f8f6f4 v[62:65], v[18:25], v[214:221], 0
	v_mfma_f32_16x16x128_f8f6f4 v[54:57], v[26:33], v[214:221], 0
	v_mfma_f32_16x16x128_f8f6f4 v[46:49], v[18:25], v[222:229], 0
	v_mfma_f32_16x16x128_f8f6f4 v[38:41], v[26:33], v[222:229], 0
	s_setprio 0
	s_setprio 1
	v_mfma_f32_16x16x128_f8f6f4 v[90:93], v[2:9], v[198:205], 0
	v_mfma_f32_16x16x128_f8f6f4 v[82:85], v[10:17], v[198:205], 0
	v_mfma_f32_16x16x128_f8f6f4 v[74:77], v[2:9], v[206:213], 0
	v_mfma_f32_16x16x128_f8f6f4 v[66:69], v[10:17], v[206:213], 0
	v_mfma_f32_16x16x128_f8f6f4 v[58:61], v[2:9], v[214:221], 0
	v_mfma_f32_16x16x128_f8f6f4 v[50:53], v[10:17], v[214:221], 0
	v_mfma_f32_16x16x128_f8f6f4 v[42:45], v[2:9], v[222:229], 0
	v_mfma_f32_16x16x128_f8f6f4 v[34:37], v[10:17], v[222:229], 0
	s_setprio 0
	s_barrier
	s_add_i32 s37, 0, 0x18000
	s_add_i32 s50, 0, 0x1c000
	v_add_u32_e32 v14, s37, v185
	v_add_u32_e32 v30, s50, v185
	ds_read_b128 v[2:5], v14
	ds_read_b128 v[6:9], v14 offset:1024
	ds_read_b128 v[10:13], v14 offset:2048
	ds_read_b128 v[14:17], v14 offset:3072
	ds_read_b128 v[18:21], v30
	ds_read_b128 v[22:25], v30 offset:1024
	ds_read_b128 v[26:29], v30 offset:2048
	ds_read_b128 v[30:33], v30 offset:3072
	s_mov_b32 m0, s61
	v_cndmask_b32_e64 v162, v168, v190, s[6:7]
	ds_read_b128 v[198:201], v188 offset:32768
	ds_read_b128 v[202:205], v188 offset:33792
	ds_read_b128 v[206:209], v188 offset:34816
	ds_read_b128 v[210:213], v188 offset:35840
	ds_read_b128 v[214:217], v188 offset:36864
	ds_read_b128 v[218:221], v188 offset:37888
	ds_read_b128 v[222:225], v188 offset:38912
	ds_read_b128 v[226:229], v188 offset:39936
	global_load_lds_dwordx4 v162, s[48:49]
	v_cndmask_b32_e64 v162, v172, v193, s[6:7]
	s_mov_b32 m0, s62
	s_nop 0
	global_load_lds_dwordx4 v162, s[48:49]
	s_waitcnt vmcnt(8)
	s_waitcnt lgkmcnt(0)
	s_barrier
	s_setprio 1
	s_waitcnt lgkmcnt(0)
	v_mfma_f32_16x16x128_f8f6f4 v[158:161], v[2:9], v[198:205], v[158:161]
	v_mfma_f32_16x16x128_f8f6f4 v[154:157], v[10:17], v[198:205], v[154:157]
	v_mfma_f32_16x16x128_f8f6f4 v[142:145], v[2:9], v[206:213], v[142:145]
	v_mfma_f32_16x16x128_f8f6f4 v[134:137], v[10:17], v[206:213], v[134:137]
	v_mfma_f32_16x16x128_f8f6f4 v[126:129], v[2:9], v[214:221], v[126:129]
	v_mfma_f32_16x16x128_f8f6f4 v[118:121], v[10:17], v[214:221], v[118:121]
	v_mfma_f32_16x16x128_f8f6f4 v[110:113], v[2:9], v[222:229], v[110:113]
	v_mfma_f32_16x16x128_f8f6f4 v[102:105], v[10:17], v[222:229], v[102:105]
	s_setprio 0
	s_setprio 1
	v_mfma_f32_16x16x128_f8f6f4 v[150:153], v[18:25], v[198:205], v[150:153]
	v_mfma_f32_16x16x128_f8f6f4 v[146:149], v[26:33], v[198:205], v[146:149]
	v_mfma_f32_16x16x128_f8f6f4 v[138:141], v[18:25], v[206:213], v[138:141]
	v_mfma_f32_16x16x128_f8f6f4 v[130:133], v[26:33], v[206:213], v[130:133]
	v_mfma_f32_16x16x128_f8f6f4 v[122:125], v[18:25], v[214:221], v[122:125]
	v_mfma_f32_16x16x128_f8f6f4 v[114:117], v[26:33], v[214:221], v[114:117]
	v_mfma_f32_16x16x128_f8f6f4 v[106:109], v[18:25], v[222:229], v[106:109]
	v_mfma_f32_16x16x128_f8f6f4 v[98:101], v[26:33], v[222:229], v[98:101]
	s_setprio 0
	s_barrier
	s_add_i32 s6, s37, s58
	v_lshl_add_u64 v[174:175], v[174:175], 0, s[16:17]
	s_mov_b32 m0, s6
	ds_read_b128 v[198:201], v188 offset:49152
	ds_read_b128 v[202:205], v188 offset:50176
	ds_read_b128 v[206:209], v188 offset:51200
	ds_read_b128 v[210:213], v188 offset:52224
	ds_read_b128 v[214:217], v188 offset:53248
	ds_read_b128 v[218:221], v188 offset:54272
	ds_read_b128 v[222:225], v188 offset:55296
	ds_read_b128 v[226:229], v188 offset:56320
	global_load_lds_dwordx4 v[174:175], off
	s_add_i32 m0, s6, 0x2000
	s_add_u32 s6, s46, 0x40080
	v_lshl_add_u64 v[174:175], v[176:177], 0, s[16:17]
	s_addc_u32 s7, s47, 0
	s_add_i32 s37, s50, s58
	global_load_lds_dwordx4 v[174:175], off
	v_lshl_add_u64 v[174:175], s[6:7], 0, v[164:165]
	s_mov_b32 m0, s37
	s_nop 0
	global_load_lds_dwordx4 v[174:175], off
	v_lshl_add_u64 v[174:175], s[6:7], 0, v[166:167]
	s_add_i32 m0, s37, 0x2000
	s_nop 0
	global_load_lds_dwordx4 v[174:175], off
	v_lshl_add_u64 v[174:175], v[178:179], 0, s[16:17]
	s_mov_b32 m0, s66
	s_nop 0
	global_load_lds_dwordx4 v[174:175], off
	v_lshl_add_u64 v[174:175], v[180:181], 0, s[16:17]
	s_mov_b32 m0, s67
	s_nop 0
	global_load_lds_dwordx4 v[174:175], off
	s_waitcnt vmcnt(8)
	s_waitcnt lgkmcnt(0)
	s_barrier
	s_setprio 1
	s_waitcnt lgkmcnt(0)
	v_mfma_f32_16x16x128_f8f6f4 v[94:97], v[2:9], v[198:205], v[94:97]
	v_mfma_f32_16x16x128_f8f6f4 v[86:89], v[10:17], v[198:205], v[86:89]
	v_mfma_f32_16x16x128_f8f6f4 v[78:81], v[2:9], v[206:213], v[78:81]
	v_mfma_f32_16x16x128_f8f6f4 v[70:73], v[10:17], v[206:213], v[70:73]
	v_mfma_f32_16x16x128_f8f6f4 v[62:65], v[2:9], v[214:221], v[62:65]
	v_mfma_f32_16x16x128_f8f6f4 v[54:57], v[10:17], v[214:221], v[54:57]
	v_mfma_f32_16x16x128_f8f6f4 v[46:49], v[2:9], v[222:229], v[46:49]
	v_mfma_f32_16x16x128_f8f6f4 v[38:41], v[10:17], v[222:229], v[38:41]
	s_setprio 0
	s_setprio 1
	v_mfma_f32_16x16x128_f8f6f4 v[90:93], v[18:25], v[198:205], v[90:93]
	v_mfma_f32_16x16x128_f8f6f4 v[82:85], v[26:33], v[198:205], v[82:85]
	v_mfma_f32_16x16x128_f8f6f4 v[74:77], v[18:25], v[206:213], v[74:77]
	v_mfma_f32_16x16x128_f8f6f4 v[66:69], v[26:33], v[206:213], v[66:69]
	v_mfma_f32_16x16x128_f8f6f4 v[58:61], v[18:25], v[214:221], v[58:61]
	v_mfma_f32_16x16x128_f8f6f4 v[50:53], v[26:33], v[214:221], v[50:53]
	v_mfma_f32_16x16x128_f8f6f4 v[42:45], v[18:25], v[222:229], v[42:45]
	v_mfma_f32_16x16x128_f8f6f4 v[34:37], v[26:33], v[222:229], v[34:37]
	s_setprio 0
	s_add_i32 s29, s29, 2
	s_add_u32 s44, s44, 0x100
	s_addc_u32 s45, s45, 0
	s_add_u32 s38, s38, 0x100
	s_addc_u32 s39, s39, 0
	s_add_u32 s50, s44, 0x80
	s_addc_u32 s51, s45, 0
	s_add_u32 s37, s44, 0x100
	s_addc_u32 s49, s45, 0
	s_add_u32 s52, s38, 0x100
	s_addc_u32 s53, s39, 0
	s_cmp_eq_u32 s29, 12
	s_cselect_b64 s[6:7], -1, 0
	s_and_b64 s[46:47], s[6:7], exec
	s_cselect_b32 s48, s40, s37
	s_cselect_b32 s49, s41, s49
	s_cselect_b32 s46, s30, s52
	s_cselect_b32 s47, s31, s53
	s_barrier
	s_branch .Lp9_body

.Lp9_body:
	v_add_u32_e32 v2, s85, v185
	v_add_u32_e32 v14, s86, v185
	ds_read_b128 v[18:21], v2
	ds_read_b128 v[22:25], v2 offset:1024
	ds_read_b128 v[26:29], v2 offset:2048
	ds_read_b128 v[30:33], v2 offset:3072
	ds_read_b128 v[2:5], v14
	ds_read_b128 v[6:9], v14 offset:1024
	ds_read_b128 v[10:13], v14 offset:2048
	ds_read_b128 v[14:17], v14 offset:3072
	v_lshl_add_u64 v[222:223], s[50:51], 0, v[168:169]
	s_add_i32 m0, s59, 0xc000
	ds_read_b128 v[174:177], v188
	ds_read_b128 v[178:181], v188 offset:1024
	ds_read_b128 v[198:201], v188 offset:2048
	ds_read_b128 v[202:205], v188 offset:3072
	ds_read_b128 v[206:209], v188 offset:4096
	ds_read_b128 v[210:213], v188 offset:5120
	ds_read_b128 v[214:217], v188 offset:6144
	ds_read_b128 v[218:221], v188 offset:7168
	global_load_lds_dwordx4 v[222:223], off
	v_lshl_add_u64 v[222:223], s[50:51], 0, v[172:173]
	s_add_i32 m0, s59, 0xe000
	s_nop 0
	global_load_lds_dwordx4 v[222:223], off
	s_waitcnt vmcnt(8)
	s_waitcnt lgkmcnt(0)
	s_barrier
	s_setprio 1
	s_waitcnt lgkmcnt(0)
	v_mfma_f32_16x16x128_f8f6f4 v[158:161], v[18:25], v[174:181], v[158:161]
	v_mfma_f32_16x16x128_f8f6f4 v[154:157], v[26:33], v[174:181], v[154:157]
	v_mfma_f32_16x16x128_f8f6f4 v[142:145], v[18:25], v[198:205], v[142:145]
	v_mfma_f32_16x16x128_f8f6f4 v[134:137], v[26:33], v[198:205], v[134:137]
	v_mfma_f32_16x16x128_f8f6f4 v[126:129], v[18:25], v[206:213], v[126:129]
	v_mfma_f32_16x16x128_f8f6f4 v[118:121], v[26:33], v[206:213], v[118:121]
	v_mfma_f32_16x16x128_f8f6f4 v[110:113], v[18:25], v[214:221], v[110:113]
	v_mfma_f32_16x16x128_f8f6f4 v[102:105], v[26:33], v[214:221], v[102:105]
	s_setprio 0
	s_setprio 1
	v_mfma_f32_16x16x128_f8f6f4 v[150:153], v[2:9], v[174:181], v[150:153]
	v_mfma_f32_16x16x128_f8f6f4 v[146:149], v[10:17], v[174:181], v[146:149]
	v_mfma_f32_16x16x128_f8f6f4 v[138:141], v[2:9], v[198:205], v[138:141]
	v_mfma_f32_16x16x128_f8f6f4 v[130:133], v[10:17], v[198:205], v[130:133]
	v_mfma_f32_16x16x128_f8f6f4 v[122:125], v[2:9], v[206:213], v[122:125]
	v_mfma_f32_16x16x128_f8f6f4 v[114:117], v[10:17], v[206:213], v[114:117]
	v_mfma_f32_16x16x128_f8f6f4 v[106:109], v[2:9], v[214:221], v[106:109]
	v_mfma_f32_16x16x128_f8f6f4 v[98:101], v[10:17], v[214:221], v[98:101]
	s_setprio 0
	s_barrier
	s_add_i32 s37, s85, s58
	v_lshl_add_u64 v[174:175], s[46:47], 0, v[164:165]
	s_mov_b32 m0, s37
	ds_read_b128 v[198:201], v188 offset:16384
	ds_read_b128 v[202:205], v188 offset:17408
	ds_read_b128 v[206:209], v188 offset:18432
	ds_read_b128 v[210:213], v188 offset:19456
	ds_read_b128 v[214:217], v188 offset:20480
	ds_read_b128 v[218:221], v188 offset:21504
	ds_read_b128 v[222:225], v188 offset:22528
	ds_read_b128 v[226:229], v188 offset:23552
	global_load_lds_dwordx4 v[174:175], off
	s_add_i32 m0, s37, 0x2000
	s_add_u32 s50, s46, 0x40000
	v_lshl_add_u64 v[176:177], s[46:47], 0, v[166:167]
	s_addc_u32 s51, s47, 0
	s_add_i32 s37, s86, s58
	global_load_lds_dwordx4 v[176:177], off
	v_lshl_add_u64 v[178:179], s[50:51], 0, v[164:165]
	s_mov_b32 m0, s37
	v_cndmask_b32_e64 v162, v196, v192, s[6:7]
	global_load_lds_dwordx4 v[178:179], off
	v_lshl_add_u64 v[178:179], s[50:51], 0, v[166:167]
	s_add_i32 m0, s37, 0x2000
	s_nop 0
	global_load_lds_dwordx4 v[178:179], off
	s_mov_b32 m0, s59
	v_lshl_add_u64 v[178:179], s[48:49], 0, v[162:163]
	global_load_lds_dwordx4 v162, s[48:49]
	v_cndmask_b32_e64 v162, v170, v191, s[6:7]
	s_mov_b32 m0, s60
	v_lshl_add_u64 v[180:181], s[48:49], 0, v[162:163]
	global_load_lds_dwordx4 v162, s[48:49]
	s_waitcnt vmcnt(8)
	s_waitcnt lgkmcnt(0)
	s_barrier
	s_setprio 1
	s_waitcnt lgkmcnt(0)
	v_mfma_f32_16x16x128_f8f6f4 v[94:97], v[18:25], v[198:205], v[94:97]
	v_mfma_f32_16x16x128_f8f6f4 v[86:89], v[26:33], v[198:205], v[86:89]
	v_mfma_f32_16x16x128_f8f6f4 v[78:81], v[18:25], v[206:213], v[78:81]
	v_mfma_f32_16x16x128_f8f6f4 v[70:73], v[26:33], v[206:213], v[70:73]
	v_mfma_f32_16x16x128_f8f6f4 v[62:65], v[18:25], v[214:221], v[62:65]
	v_mfma_f32_16x16x128_f8f6f4 v[54:57], v[26:33], v[214:221], v[54:57]
	v_mfma_f32_16x16x128_f8f6f4 v[46:49], v[18:25], v[222:229], v[46:49]
	v_mfma_f32_16x16x128_f8f6f4 v[38:41], v[26:33], v[222:229], v[38:41]
	s_setprio 0
	s_setprio 1
	v_mfma_f32_16x16x128_f8f6f4 v[90:93], v[2:9], v[198:205], v[90:93]
	v_mfma_f32_16x16x128_f8f6f4 v[82:85], v[10:17], v[198:205], v[82:85]
	v_mfma_f32_16x16x128_f8f6f4 v[74:77], v[2:9], v[206:213], v[74:77]
	v_mfma_f32_16x16x128_f8f6f4 v[66:69], v[10:17], v[206:213], v[66:69]
	v_mfma_f32_16x16x128_f8f6f4 v[58:61], v[2:9], v[214:221], v[58:61]
	v_mfma_f32_16x16x128_f8f6f4 v[50:53], v[10:17], v[214:221], v[50:53]
	v_mfma_f32_16x16x128_f8f6f4 v[42:45], v[2:9], v[222:229], v[42:45]
	v_mfma_f32_16x16x128_f8f6f4 v[34:37], v[10:17], v[222:229], v[34:37]
	s_setprio 0
	s_barrier
	s_add_i32 s37, 0, 0x18000
	s_add_i32 s50, 0, 0x1c000
	v_add_u32_e32 v14, s37, v185
	v_add_u32_e32 v30, s50, v185
	ds_read_b128 v[2:5], v14
	ds_read_b128 v[6:9], v14 offset:1024
	ds_read_b128 v[10:13], v14 offset:2048
	ds_read_b128 v[14:17], v14 offset:3072
	ds_read_b128 v[18:21], v30
	ds_read_b128 v[22:25], v30 offset:1024
	ds_read_b128 v[26:29], v30 offset:2048
	ds_read_b128 v[30:33], v30 offset:3072
	s_mov_b32 m0, s61
	v_cndmask_b32_e64 v162, v168, v190, s[6:7]
	ds_read_b128 v[198:201], v188 offset:32768
	ds_read_b128 v[202:205], v188 offset:33792
	ds_read_b128 v[206:209], v188 offset:34816
	ds_read_b128 v[210:213], v188 offset:35840
	ds_read_b128 v[214:217], v188 offset:36864
	ds_read_b128 v[218:221], v188 offset:37888
	ds_read_b128 v[222:225], v188 offset:38912
	ds_read_b128 v[226:229], v188 offset:39936
	global_load_lds_dwordx4 v162, s[48:49]
	v_cndmask_b32_e64 v162, v172, v193, s[6:7]
	s_mov_b32 m0, s62
	s_nop 0
	global_load_lds_dwordx4 v162, s[48:49]
	s_waitcnt vmcnt(8)
	s_waitcnt lgkmcnt(0)
	s_barrier
	s_setprio 1
	s_waitcnt lgkmcnt(0)
	v_mfma_f32_16x16x128_f8f6f4 v[158:161], v[2:9], v[198:205], v[158:161]
	v_mfma_f32_16x16x128_f8f6f4 v[154:157], v[10:17], v[198:205], v[154:157]
	v_mfma_f32_16x16x128_f8f6f4 v[142:145], v[2:9], v[206:213], v[142:145]
	v_mfma_f32_16x16x128_f8f6f4 v[134:137], v[10:17], v[206:213], v[134:137]
	v_mfma_f32_16x16x128_f8f6f4 v[126:129], v[2:9], v[214:221], v[126:129]
	v_mfma_f32_16x16x128_f8f6f4 v[118:121], v[10:17], v[214:221], v[118:121]
	v_mfma_f32_16x16x128_f8f6f4 v[110:113], v[2:9], v[222:229], v[110:113]
	v_mfma_f32_16x16x128_f8f6f4 v[102:105], v[10:17], v[222:229], v[102:105]
	s_setprio 0
	s_setprio 1
	v_mfma_f32_16x16x128_f8f6f4 v[150:153], v[18:25], v[198:205], v[150:153]
	v_mfma_f32_16x16x128_f8f6f4 v[146:149], v[26:33], v[198:205], v[146:149]
	v_mfma_f32_16x16x128_f8f6f4 v[138:141], v[18:25], v[206:213], v[138:141]
	v_mfma_f32_16x16x128_f8f6f4 v[130:133], v[26:33], v[206:213], v[130:133]
	v_mfma_f32_16x16x128_f8f6f4 v[122:125], v[18:25], v[214:221], v[122:125]
	v_mfma_f32_16x16x128_f8f6f4 v[114:117], v[26:33], v[214:221], v[114:117]
	v_mfma_f32_16x16x128_f8f6f4 v[106:109], v[18:25], v[222:229], v[106:109]
	v_mfma_f32_16x16x128_f8f6f4 v[98:101], v[26:33], v[222:229], v[98:101]
	s_setprio 0
	s_barrier
	s_add_i32 s6, s37, s58
	v_lshl_add_u64 v[174:175], v[174:175], 0, s[16:17]
	s_mov_b32 m0, s6
	ds_read_b128 v[198:201], v188 offset:49152
	ds_read_b128 v[202:205], v188 offset:50176
	ds_read_b128 v[206:209], v188 offset:51200
	ds_read_b128 v[210:213], v188 offset:52224
	ds_read_b128 v[214:217], v188 offset:53248
	ds_read_b128 v[218:221], v188 offset:54272
	ds_read_b128 v[222:225], v188 offset:55296
	ds_read_b128 v[226:229], v188 offset:56320
	global_load_lds_dwordx4 v[174:175], off
	s_add_i32 m0, s6, 0x2000
	s_add_u32 s6, s46, 0x40080
	v_lshl_add_u64 v[174:175], v[176:177], 0, s[16:17]
	s_addc_u32 s7, s47, 0
	s_add_i32 s37, s50, s58
	global_load_lds_dwordx4 v[174:175], off
	v_lshl_add_u64 v[174:175], s[6:7], 0, v[164:165]
	s_mov_b32 m0, s37
	s_nop 0
	global_load_lds_dwordx4 v[174:175], off
	v_lshl_add_u64 v[174:175], s[6:7], 0, v[166:167]
	s_add_i32 m0, s37, 0x2000
	s_nop 0
	global_load_lds_dwordx4 v[174:175], off
	v_lshl_add_u64 v[174:175], v[178:179], 0, s[16:17]
	s_mov_b32 m0, s66
	s_nop 0
	global_load_lds_dwordx4 v[174:175], off
	v_lshl_add_u64 v[174:175], v[180:181], 0, s[16:17]
	s_mov_b32 m0, s67
	s_nop 0
	global_load_lds_dwordx4 v[174:175], off
	s_waitcnt vmcnt(8)
	s_waitcnt lgkmcnt(0)
	s_barrier
	s_setprio 1
	s_waitcnt lgkmcnt(0)
	v_mfma_f32_16x16x128_f8f6f4 v[94:97], v[2:9], v[198:205], v[94:97]
	v_mfma_f32_16x16x128_f8f6f4 v[86:89], v[10:17], v[198:205], v[86:89]
	v_mfma_f32_16x16x128_f8f6f4 v[78:81], v[2:9], v[206:213], v[78:81]
	v_mfma_f32_16x16x128_f8f6f4 v[70:73], v[10:17], v[206:213], v[70:73]
	v_mfma_f32_16x16x128_f8f6f4 v[62:65], v[2:9], v[214:221], v[62:65]
	v_mfma_f32_16x16x128_f8f6f4 v[54:57], v[10:17], v[214:221], v[54:57]
	v_mfma_f32_16x16x128_f8f6f4 v[46:49], v[2:9], v[222:229], v[46:49]
	v_mfma_f32_16x16x128_f8f6f4 v[38:41], v[10:17], v[222:229], v[38:41]
	s_setprio 0
	s_setprio 1
	v_mfma_f32_16x16x128_f8f6f4 v[90:93], v[18:25], v[198:205], v[90:93]
	v_mfma_f32_16x16x128_f8f6f4 v[82:85], v[26:33], v[198:205], v[82:85]
	v_mfma_f32_16x16x128_f8f6f4 v[74:77], v[18:25], v[206:213], v[74:77]
	v_mfma_f32_16x16x128_f8f6f4 v[66:69], v[26:33], v[206:213], v[66:69]
	v_mfma_f32_16x16x128_f8f6f4 v[58:61], v[18:25], v[214:221], v[58:61]
	v_mfma_f32_16x16x128_f8f6f4 v[50:53], v[26:33], v[214:221], v[50:53]
	v_mfma_f32_16x16x128_f8f6f4 v[42:45], v[18:25], v[222:229], v[42:45]
	v_mfma_f32_16x16x128_f8f6f4 v[34:37], v[26:33], v[222:229], v[34:37]
	s_setprio 0
	s_add_i32 s29, s29, 2
	s_add_u32 s44, s44, 0x100
	s_addc_u32 s45, s45, 0
	s_add_u32 s38, s38, 0x100
	s_addc_u32 s39, s39, 0
	s_cmp_gt_u32 s29, 13
	s_cbranch_scc1 .Lp9_exitb
	s_add_u32 s50, s44, 0x80
	s_addc_u32 s51, s45, 0
	s_add_u32 s37, s44, 0x100
	s_addc_u32 s49, s45, 0
	s_add_u32 s52, s38, 0x100
	s_addc_u32 s53, s39, 0
	s_cmp_eq_u32 s29, 12
	s_cselect_b64 s[6:7], -1, 0
	s_and_b64 s[46:47], s[6:7], exec
	s_cselect_b32 s48, s40, s37
	s_cselect_b32 s49, s41, s49
	s_cselect_b32 s46, s30, s52
	s_cselect_b32 s47, s31, s53
	s_barrier
	s_cmp_lt_i32 s29, 10
	s_cbranch_scc1 .Lp9_body
	s_branch .Lp9_ge10

.Lp9_ge10:
	s_cmp_lg_u32 s29, 12
	s_cbranch_scc1 .Lp9_nofin
	s_andn2_b64 vcc, exec, s[4:5]
	s_cbranch_vccnz .Lp9_nofin
	v_lshl_add_u32 v192, v230, 11, v183
	v_lshl_add_u32 v191, v231, 11, v184
	v_lshl_add_u32 v190, v232, 11, v183
	v_lshl_add_u32 v193, v233, 11, v184

.LBB0_1367:
	s_add_u32 s30, s38, 0x100
	s_addc_u32 s31, s39, 0
	s_ashr_i32 s27, s26, 31
	s_cbranch_execz .LBB0_1352
	s_branch .LBB0_1353
.Lp9_exitb:
	s_barrier
.LBB0_1368:
.LBB0_1370:
	s_ashr_i32 s37, s36, 31
	s_lshl_b64 s[6:7], s[36:37], 14
	v_lshl_or_b32 v22, s34, 7, v186
	s_add_u32 s6, s10, s6
	s_addc_u32 s7, s11, s7
	v_ashrrev_i32_e32 v23, 31, v22
	s_mov_b64 s[6:7], 0x2000
	v_lshl_add_u32 v18, v195, 8, v171
	v_or_b32_e32 v24, 16, v18
	v_or_b32_e32 v26, 32, v18
	v_or_b32_e32 v28, 48, v18
	v_ashrrev_i32_e32 v19, 31, v18
	v_ashrrev_i32_e32 v25, 31, v24
	v_ashrrev_i32_e32 v27, 31, v26
	v_ashrrev_i32_e32 v29, 31, v28
	v_lshlrev_b64 v[18:19], 11, v[18:19]
	v_lshlrev_b64 v[24:25], 11, v[24:25]
	v_lshlrev_b64 v[26:27], 11, v[26:27]
	v_lshlrev_b64 v[28:29], 11, v[28:29]
	v_lshl_add_u64 v[18:19], s[14:15], 0, v[18:19]
	v_lshl_add_u64 v[24:25], s[14:15], 0, v[24:25]
	v_lshl_add_u64 v[26:27], s[14:15], 0, v[26:27]
	v_lshl_add_u64 v[28:29], s[14:15], 0, v[28:29]
	v_lshl_add_u64 v[18:19], v[18:19], 0, v[22:23]
	v_lshl_add_u64 v[24:25], v[24:25], 0, v[22:23]
	v_lshl_add_u64 v[26:27], v[26:27], 0, v[22:23]
	v_lshl_add_u64 v[22:23], v[28:29], 0, v[22:23]
	v_mov_b32_e32 v20, v163
	v_mov_b32_e32 v21, v163
	s_mov_b32 s6, 0x40000
	v_mov_b64_e32 v[6:7], v[234:235]
	v_mov_b64_e32 v[8:9], v[236:237]
	v_mov_b64_e32 v[14:15], v[238:239]
	v_mov_b64_e32 v[16:17], v[240:241]
	v_mov_b64_e32 v[10:11], v[242:243]
	v_mov_b64_e32 v[12:13], v[244:245]
	v_mov_b64_e32 v[2:3], v[246:247]
	v_mov_b64_e32 v[4:5], v[248:249]
	v_pk_fma_f32 v[32:33], v[154:155], s[22:23], v[6:7] op_sel_hi:[1,0,1]
	v_pk_fma_f32 v[28:29], v[158:159], s[22:23], v[14:15] op_sel_hi:[1,0,1]
	v_pk_fma_f32 v[154:155], v[156:157], s[22:23], v[8:9] op_sel_hi:[1,0,1]
	v_min_f32_e32 v28, 0x40e00000, v28
	v_min_f32_e32 v29, 0x40e00000, v29
	v_min_f32_e32 v32, 0x40e00000, v32
	v_min_f32_e32 v33, 0x40e00000, v33
	v_pk_mul_f32 v[156:157], v[28:29], s[24:25] op_sel_hi:[1,0]
	v_pk_fma_f32 v[30:31], v[160:161], s[22:23], v[16:17] op_sel_hi:[1,0,1]
	v_pk_mul_f32 v[160:161], v[32:33], s[24:25] op_sel_hi:[1,0]
	v_exp_f32_e32 v156, v156
	v_exp_f32_e32 v157, v157
	v_exp_f32_e32 v160, v160
	v_exp_f32_e32 v161, v161
	v_min_f32_e32 v30, 0x40e00000, v30
	v_min_f32_e32 v31, 0x40e00000, v31
	v_min_f32_e32 v154, 0x40e00000, v154
	v_min_f32_e32 v155, 0x40e00000, v155
	v_pk_mul_f32 v[158:159], v[30:31], s[24:25] op_sel_hi:[1,0]
	v_pk_mul_f32 v[168:169], v[154:155], s[24:25] op_sel_hi:[1,0]
	v_exp_f32_e32 v158, v158
	v_exp_f32_e32 v159, v159
	v_pk_add_f32 v[156:157], v[156:157], 1.0 op_sel_hi:[1,0]
	v_exp_f32_e32 v168, v168
	v_exp_f32_e32 v169, v169
	v_pk_add_f32 v[160:161], v[160:161], 1.0 op_sel_hi:[1,0]
	v_rcp_f32_e32 v156, v156
	v_rcp_f32_e32 v157, v157
	v_rcp_f32_e32 v160, v160
	v_rcp_f32_e32 v161, v161
	v_pk_fma_f32 v[150:151], v[150:151], s[22:23], v[10:11] op_sel_hi:[1,0,1]
	v_pk_fma_f32 v[146:147], v[146:147], s[22:23], v[2:3] op_sel_hi:[1,0,1]
	v_med3_f32 v150, v150, s87, v189
	v_med3_f32 v151, v151, s87, v189
	v_pk_add_f32 v[158:159], v[158:159], 1.0 op_sel_hi:[1,0]
	v_med3_f32 v146, v146, s87, v189
	v_med3_f32 v147, v147, s87, v189
	v_pk_add_f32 v[150:151], v[150:151], 1.0 op_sel_hi:[1,0]
	v_pk_add_f32 v[168:169], v[168:169], 1.0 op_sel_hi:[1,0]
	v_rcp_f32_e32 v158, v158
	v_rcp_f32_e32 v159, v159
	v_pk_mul_f32 v[28:29], v[28:29], v[156:157]
	v_pk_add_f32 v[146:147], v[146:147], 1.0 op_sel_hi:[1,0]
	v_rcp_f32_e32 v168, v168
	v_rcp_f32_e32 v169, v169
	v_pk_mul_f32 v[32:33], v[32:33], v[160:161]
	v_pk_mul_f32 v[28:29], v[150:151], v[28:29]
	v_pk_fma_f32 v[152:153], v[152:153], s[22:23], v[12:13] op_sel_hi:[1,0,1]
	v_pk_mul_f32 v[32:33], v[146:147], v[32:33]
	v_cvt_pk_fp8_f32 v20, v28, v29
	v_pk_fma_f32 v[148:149], v[148:149], s[22:23], v[4:5] op_sel_hi:[1,0,1]
	v_med3_f32 v152, v152, s87, v189
	v_med3_f32 v153, v153, s87, v189
	v_cvt_pk_fp8_f32 v21, v32, v33
	v_med3_f32 v148, v148, s87, v189
	v_med3_f32 v149, v149, s87, v189
	v_pk_add_f32 v[152:153], v[152:153], 1.0 op_sel_hi:[1,0]
	v_pk_mul_f32 v[30:31], v[30:31], v[158:159]
	v_pk_fma_f32 v[142:143], v[142:143], s[22:23], v[14:15] op_sel_hi:[1,0,1]
	v_pk_add_f32 v[148:149], v[148:149], 1.0 op_sel_hi:[1,0]
	v_pk_mul_f32 v[154:155], v[154:155], v[168:169]
	v_pk_mul_f32 v[28:29], v[152:153], v[30:31]
	v_pk_mul_f32 v[30:31], v[148:149], v[154:155]
	v_cvt_pk_fp8_f32 v20, v28, v29 op_sel:[0,0,1]
	v_min_f32_e32 v28, 0x40e00000, v142
	v_min_f32_e32 v29, 0x40e00000, v143
	v_cvt_pk_fp8_f32 v21, v30, v31 op_sel:[0,0,1]
	v_pk_mul_f32 v[30:31], v[28:29], s[24:25] op_sel_hi:[1,0]
	v_pk_fma_f32 v[32:33], v[138:139], s[22:23], v[10:11] op_sel_hi:[1,0,1]
	v_exp_f32_e32 v30, v30
	s_and_b64 vcc, exec, s[18:19]
	s_cbranch_vccz .Lp9_lbar
	s_barrier
